# per-region priority A/B: v58 with the raise swapped to waves 4-7 inside the attention loop only
# baseline (speedup 1.0000x reference)
.LBB0_1343:
	s_and_b32 s3, s21, 3
	s_and_b64 s[4:5], exec, s[34:35]
	s_cselect_b32 s3, -1, s3
	s_cmp_eq_u32 s3, 2
	s_movk_i32 s4, 0x3080
	s_cselect_b32 s4, 0x2000, s4
	s_cmp_lg_u32 s3, 1
	s_cselect_b32 s4, s4, 0x1000
	s_cmp_gt_i32 s3, 0
	s_cselect_b32 s8, s4, 0
	s_mul_i32 s18, s8, 0xe00
	v_readlane_b32 s4, v253, 7
	v_readlane_b32 s5, v253, 8
	s_add_u32 s4, s4, s18
	v_lshlrev_b32_e32 v2, 8, v181
	v_mov_b32_e32 v3, v99
	v_lshl_add_u32 v7, v7, 7, v14
	s_addc_u32 s5, s5, 0
	v_lshlrev_b64 v[50:51], 1, v[2:3]
	v_cvt_pk_bf16_f32 v5, v5, v99
	ds_write_b16 v7, v5
	v_cvt_pk_bf16_f32 v4, v4, v99
	v_lshl_add_u64 v[2:3], s[4:5], 0, v[50:51]
	ds_write_b16 v7, v4 offset:32
	v_ashrrev_i32_e32 v4, 4, v6
	v_lshlrev_b32_e32 v5, 3, v6
	s_movk_i32 s4, 0x700
	v_and_b32_e32 v7, 0x78, v5
	v_mul_lo_u32 v8, v4, s4
	v_or_b32_e32 v8, v8, v7
	v_lshlrev_b32_e32 v52, 1, v8
	v_readfirstlane_b32 s4, v2
	v_readfirstlane_b32 s5, v3
	s_waitcnt lgkmcnt(0)
	s_barrier
	v_add_u32_e32 v54, 0x1c000, v52
	s_nop 1
	global_load_dwordx4 v[8:11], v52, s[4:5] offset:1792
	global_load_dwordx4 v[14:17], v54, s[4:5] offset:1792
	s_lshl_b32 s22, s8, 7
	v_readlane_b32 s8, v253, 5
	v_lshlrev_b32_e32 v26, 4, v6
	v_readlane_b32 s9, v253, 6
	s_add_u32 s24, s8, s22
	v_ashrrev_i32_e32 v13, 3, v6
	v_and_b32_e32 v30, 0x70, v26
	s_addc_u32 s25, s9, 0
	v_lshl_or_b32 v56, v13, 7, v30
	global_load_dwordx4 v[18:21], v52, s[4:5] offset:1536
	global_load_dwordx4 v[22:25], v54, s[4:5] offset:1536
	global_load_dwordx4 v[26:29], v56, s[24:25]
	v_lshlrev_b32_e32 v31, 7, v194
	v_lshlrev_b32_e32 v12, 1, v12
	v_readlane_b32 s4, v255, 34
	v_lshlrev_b32_e32 v32, 1, v4
	v_lshrrev_b32_e32 v33, 1, v4
	v_add3_u32 v12, s4, v31, v12
	v_and_b32_e32 v31, 0xfffff0, v4
	v_and_b32_e32 v35, 3, v4
	v_add_u32_e32 v36, 32, v4
	s_add_i32 s4, 0, 0x14000
	ds_read_b128 v[144:147], v12
	ds_read_b128 v[140:143], v12 offset:32
	ds_read_b128 v[136:139], v12 offset:64
	ds_read_b128 v[132:135], v12 offset:96
	v_and_or_b32 v12, v32, 8, v31
	v_and_or_b32 v31, v33, 4, v35
	v_and_b32_e32 v32, 0xfffff0, v36
	v_lshlrev_b32_e32 v33, 1, v36
	s_and_b64 s[0:1], s[0:1], exec
	v_bfe_u32 v34, v5, 5, 2
	v_lshrrev_b32_e32 v12, 1, v12
	v_and_or_b32 v32, v33, 8, v32
	s_cselect_b32 s5, 0x104, 4
	s_cmp_lt_u32 s3, 2
	v_lshlrev_b32_e32 v7, 1, v7
	v_or_b32_e32 v12, v12, v34
	v_lshrrev_b32_e32 v32, 1, v32
	s_cselect_b32 s3, 64, 0x42
	s_and_b64 s[0:1], exec, s[34:35]
	v_lshlrev_b32_e32 v31, 6, v31
	v_and_b32_e32 v35, 48, v7
	v_lshlrev_b32_e32 v12, 9, v12
	v_or_b32_e32 v32, v32, v34
	s_cselect_b32 s3, s5, s3
	s_add_i32 s0, 0, 0x8000
	v_lshlrev_b32_e32 v32, 9, v32
	v_or3_b32 v12, v12, v31, v35
	s_cmp_lg_u32 s0, -1
	v_or3_b32 v31, v32, v31, v35
	v_add_u32_e32 v205, 0, v12
	s_cselect_b32 s0, s0, 0
	s_movk_i32 s8, 0x70
	v_add_u32_e32 v206, 0, v31
	s_waitcnt vmcnt(0)
	v_mov_b32_e32 v12, s0
	s_movk_i32 s0, 0x180
	v_mul_lo_u32 v4, v4, s0
	v_bitop3_b32 v37, v98, v5, s8 bitop3:0x78
	s_waitcnt vmcnt(4)
	ds_write_b128 v205, v[8:11]
	s_waitcnt vmcnt(3)
	ds_write_b128 v206, v[14:17]
	v_lshrrev_b32_e32 v8, 1, v6
	v_bitop3_b32 v7, v7, v8, s8 bitop3:0x78
	v_add3_u32 v207, v7, v4, 0
	v_mul_lo_u32 v4, v13, s0
	v_or_b32_e32 v7, 0x100, v30
	v_and_b32_e32 v8, 0x70, v6
	v_mad_u32_u24 v53, v195, s0, v12
	v_xad_u32 v4, v7, v8, v4
	v_add_u32_e32 v201, v37, v53
	v_add_u32_e32 v208, 0, v4
	s_waitcnt vmcnt(2)
	ds_write_b128 v207, v[18:21] offset:32768
	s_waitcnt vmcnt(1)
	ds_write_b128 v207, v[22:25] offset:45056
	s_waitcnt vmcnt(0)
	ds_write_b128 v208, v[26:29] offset:32768
	s_waitcnt lgkmcnt(0)
	s_barrier
	ds_read_b128 v[8:11], v201
	ds_read_b128 v[12:15], v201 offset:128
	s_waitcnt lgkmcnt(1)
	v_mfma_f32_32x32x16_bf16 v[18:33], v[8:11], v[128:131], 0
	ds_read_b128 v[8:11], v201 offset:12288
	ds_read_b128 v[60:63], v201 offset:256
	v_and_b32_e32 v4, 0x70, v5
	v_bitop3_b32 v5, v98, v4, 32 bitop3:0x36
	v_add_u32_e32 v203, v5, v53
	v_bitop3_b32 v5, v98, v4, 64 bitop3:0x36
	v_add_u32_e32 v204, v5, v53
	s_waitcnt lgkmcnt(1)
	v_mfma_f32_32x32x16_bf16 v[34:49], v[8:11], v[128:131], 0
	ds_read_b128 v[8:11], v203
	ds_read_b128 v[64:67], v203 offset:128
	ds_read_b128 v[68:71], v203 offset:256
	s_movk_i32 s0, 0x60
	v_bitop3_b32 v4, v98, v4, s0 bitop3:0x36
	v_add_u32_e32 v202, v4, v53
	s_mov_b64 s[0:1], 0x38700
	v_lshl_add_u64 v[4:5], v[2:3], 0, s[0:1]
	s_waitcnt lgkmcnt(2)
	v_mfma_f32_32x32x16_bf16 v[18:33], v[8:11], v[124:127], v[18:33]
	ds_read_b128 v[8:11], v203 offset:12288
	s_mov_b64 s[0:1], 0x38600
	v_lshl_add_u64 v[2:3], v[2:3], 0, s[0:1]
	v_readfirstlane_b32 s0, v4
	v_readfirstlane_b32 s1, v5
	v_readfirstlane_b32 s8, v2
	v_readfirstlane_b32 s9, v3
	s_waitcnt lgkmcnt(0)
	v_mfma_f32_32x32x16_bf16 v[34:49], v[8:11], v[124:127], v[34:49]
	ds_read_b128 v[8:11], v204
	ds_read_b128 v[72:75], v204 offset:128
	ds_read_b128 v[76:79], v204 offset:256
	v_mov_b32_e32 v57, v99
	v_add_u32_e32 v209, 0x3000, v207
	s_cmp_lg_u32 0, -1
	v_lshlrev_b32_e32 v4, 1, v58
	v_and_b32_e32 v4, 32, v4
	s_waitcnt lgkmcnt(2)
	v_mfma_f32_32x32x16_bf16 v[18:33], v[8:11], v[120:123], v[18:33]
	ds_read_b128 v[8:11], v204 offset:12288
	s_mov_b32 s36, s63
	s_mov_b32 s37, s63
	s_mov_b32 s19, s63
	s_mov_b32 s38, s63
	s_mov_b32 s39, s63
	s_mov_b32 s40, s63
	s_waitcnt lgkmcnt(0)
	v_mfma_f32_32x32x16_bf16 v[34:49], v[8:11], v[120:123], v[34:49]
	ds_read_b128 v[8:11], v202
	ds_read_b128 v[80:83], v202 offset:128
	s_mov_b32 s41, s63
	s_mov_b32 s42, s63
	s_mov_b32 s43, s63
	s_mov_b32 s44, s63
	s_mov_b32 s45, s63
	s_mov_b32 s46, s63
	s_waitcnt lgkmcnt(1)
	v_mfma_f32_32x32x16_bf16 v[18:33], v[8:11], v[116:119], v[18:33]
	ds_read_b128 v[8:11], v202 offset:12288
	ds_read_b128 v[84:87], v202 offset:256
	s_mov_b32 s47, s63
	s_mov_b32 s48, s63
	s_mov_b32 s49, s63
	s_mov_b32 s50, s63
	s_mov_b32 s51, s63
	s_mov_b32 s23, s63
	v_mfma_f32_32x32x16_bf16 v[18:33], v[12:15], v[112:115], v[18:33]
	v_mov_b32_e32 v53, v99
	v_mov_b32_e32 v55, v99
	v_lshl_add_u64 v[182:183], s[22:23], 0, v[56:57]
	v_mov_b32_e32 v227, 0x3200
	v_mov_b32_e32 v199, 0
	s_waitcnt lgkmcnt(1)
	v_mfma_f32_32x32x16_bf16 v[34:49], v[8:11], v[116:119], v[34:49]
	ds_read_b128 v[8:11], v201 offset:12416
	ds_read_b128 v[12:15], v201 offset:12544
	v_mfma_f32_32x32x16_bf16 v[18:33], v[64:67], v[108:111], v[18:33]
	s_waitcnt lgkmcnt(1)
	v_mfma_f32_32x32x16_bf16 v[34:49], v[8:11], v[112:115], v[34:49]
	ds_read_b128 v[8:11], v203 offset:12416
	ds_read_b128 v[64:67], v203 offset:12544
	v_mfma_f32_32x32x16_bf16 v[18:33], v[72:75], v[104:107], v[18:33]
	s_waitcnt lgkmcnt(1)
	v_mfma_f32_32x32x16_bf16 v[34:49], v[8:11], v[108:111], v[34:49]
	ds_read_b128 v[8:11], v204 offset:12416
	ds_read_b128 v[72:75], v204 offset:12544
	v_mfma_f32_32x32x16_bf16 v[18:33], v[80:83], v[100:103], v[18:33]
	s_waitcnt lgkmcnt(1)
	v_mfma_f32_32x32x16_bf16 v[34:49], v[8:11], v[104:107], v[34:49]
	ds_read_b128 v[8:11], v202 offset:12416
	ds_read_b128 v[80:83], v202 offset:12544
	v_mfma_f32_32x32x16_bf16 v[18:33], v[60:63], v[144:147], v[18:33]
	global_load_dwordx4 v[60:63], v54, s[0:1]
	global_load_dwordx4 v[88:91], v52, s[8:9]
	global_load_dwordx4 v[92:95], v52, s[0:1]
	global_load_dwordx4 v[148:151], v54, s[8:9]
	s_movk_i32 s0, 0x2000
	s_mov_b32 s8, 2
	s_waitcnt lgkmcnt(1)
	v_mfma_f32_32x32x16_bf16 v[34:49], v[8:11], v[100:103], v[34:49]
	v_lshl_add_u64 v[8:9], s[24:25], 0, v[56:57]
	v_add_co_u32_e32 v2, vcc, s0, v8
	v_cmp_gt_u32_e64 s[0:1], 32, v58
	s_nop 0
	v_addc_co_u32_e32 v3, vcc, 0, v9, vcc
	global_load_dwordx4 v[152:155], v[2:3], off
	v_mfma_f32_32x32x16_bf16 v[18:33], v[68:71], v[140:143], v[18:33]
	s_waitcnt vmcnt(0)
	s_waitcnt vmcnt(2)
	ds_write_b128 v205, v[92:95] offset:16384
	ds_write_b128 v206, v[60:63] offset:16384
	ds_write_b128 v207, v[88:91] offset:57344
	s_waitcnt vmcnt(1)
	ds_write_b128 v209, v[148:151] offset:57344
	s_waitcnt vmcnt(0)
	ds_write_b128 v208, v[152:155] offset:57344
	v_mfma_f32_32x32x16_bf16 v[34:49], v[12:15], v[144:147], v[34:49]
	v_and_b32_e32 v2, 0x3fffffc0, v6
	v_lshl_add_u32 v196, v2, 2, s4
	s_cselect_b32 s4, 0, 0
	v_lshlrev_b32_e32 v3, 4, v58
	v_lshlrev_b32_e32 v2, 3, v58
	v_and_b32_e32 v3, 0xc0, v3
	v_and_or_b32 v3, v2, 24, v3
	v_mfma_f32_32x32x16_bf16 v[18:33], v[76:79], v[136:139], v[18:33]
	v_and_b32_e32 v2, 0x100, v2
	v_or3_b32 v59, v3, v4, v2
	v_mov_b64_e32 v[2:3], s[36:37]
	v_add_u32_e32 v200, s4, v59
	v_mov_b64_e32 v[16:17], s[50:51]
	v_mov_b64_e32 v[4:5], s[38:39]
	v_mov_b64_e32 v[6:7], s[40:41]
	v_mfma_f32_32x32x16_bf16 v[34:49], v[64:67], v[140:143], v[34:49]
	v_mov_b64_e32 v[8:9], s[42:43]
	v_mov_b64_e32 v[10:11], s[44:45]
	v_mov_b64_e32 v[12:13], s[46:47]
	v_mov_b64_e32 v[14:15], s[48:49]
	v_lshl_add_u32 v197, v195, 2, v196
	s_waitcnt lgkmcnt(0)
	s_barrier
	v_mfma_f32_32x32x16_bf16 v[18:33], v[84:87], v[132:135], v[18:33]
	v_mfma_f32_32x32x16_bf16 v[34:49], v[72:75], v[136:139], v[34:49]
	s_nop 10
	v_max_f32_e32 v64, v19, v19
	v_max_f32_e32 v65, v18, v18
	v_max_f32_e32 v64, v65, v64
	v_max3_f32 v64, v64, v20, v21
	v_max3_f32 v64, v64, v22, v23
	v_max3_f32 v64, v64, v24, v25
	v_max3_f32 v64, v64, v26, v27
	v_mfma_f32_32x32x16_bf16 v[34:49], v[80:83], v[132:135], v[34:49]
	v_max3_f32 v64, v64, v28, v29
	v_max3_f32 v64, v64, v30, v31
	v_max3_f32 v64, v64, v32, v33
	s_nop 8
	v_max3_f32 v64, v64, v34, v35
	v_max3_f32 v64, v64, v36, v37
	v_max3_f32 v64, v64, v38, v39
	v_max3_f32 v64, v64, v40, v41
	v_max3_f32 v64, v64, v42, v43
	v_max3_f32 v64, v64, v44, v45
	v_max3_f32 v64, v64, v46, v47
	v_max3_f32 v64, v64, v48, v49
	v_mov_b32_e32 v65, v64
	s_nop 1
	v_permlane32_swap_b32_e32 v64, v65
	v_max_f32_e32 v65, v65, v65
	v_max_f32_e32 v64, v64, v64
	v_max_f32_e32 v64, v64, v65
	v_max_f32_e32 v60, 0xf149f2ca, v64
	v_sub_f32_e32 v61, 0xf149f2ca, v60
	v_mul_f32_e32 v61, 0x3dd53b94, v61
	v_add_f32_e32 v65, 0x7149f2ca, v64
	v_exp_f32_e32 v61, v61
	v_cmp_ge_f32_e32 vcc, s11, v65
	s_cmp_eq_u64 vcc, exec
	s_cselect_b64 vcc, -1, 0
	v_cndmask_b32_e64 v210, v61, 1.0, vcc
	v_mov_b32_e32 v61, 0xf149f2ca
	v_cndmask_b32_e32 v211, v60, v61, vcc
	v_mul_f32_e32 v60, 0xbdd53b94, v211
	v_fmamk_f32 v18, v18, 0x3dd53b94, v60
	v_exp_f32_e32 v169, v18
	v_fmamk_f32 v18, v19, 0x3dd53b94, v60
	v_exp_f32_e32 v191, v18
	v_fmamk_f32 v18, v20, 0x3dd53b94, v60
	v_exp_f32_e32 v170, v18
	v_fmamk_f32 v18, v21, 0x3dd53b94, v60
	v_exp_f32_e32 v192, v18
	v_fmamk_f32 v18, v22, 0x3dd53b94, v60
	v_exp_f32_e32 v190, v18
	v_fmamk_f32 v18, v23, 0x3dd53b94, v60
	v_exp_f32_e32 v193, v18
	v_fmamk_f32 v18, v24, 0x3dd53b94, v60
	v_exp_f32_e32 v171, v18
	v_fmamk_f32 v18, v25, 0x3dd53b94, v60
	v_exp_f32_e32 v189, v18
	v_fmamk_f32 v18, v26, 0x3dd53b94, v60
	v_exp_f32_e32 v173, v18
	v_fmamk_f32 v18, v27, 0x3dd53b94, v60
	v_exp_f32_e32 v175, v18
	v_fmamk_f32 v18, v28, 0x3dd53b94, v60
	v_exp_f32_e32 v174, v18
	v_fmamk_f32 v18, v29, 0x3dd53b94, v60
	v_exp_f32_e32 v188, v18
	v_fmamk_f32 v18, v30, 0x3dd53b94, v60
	v_exp_f32_e32 v164, v18
	v_fmamk_f32 v18, v31, 0x3dd53b94, v60
	v_pk_fma_f32 v[148:149], v[48:49], s[56:57], v[60:61] op_sel_hi:[1,0,0]
	v_pk_fma_f32 v[154:155], v[46:47], s[56:57], v[60:61] op_sel_hi:[1,0,0]
	v_pk_fma_f32 v[158:159], v[44:45], s[56:57], v[60:61] op_sel_hi:[1,0,0]
	v_pk_fma_f32 v[150:151], v[42:43], s[56:57], v[60:61] op_sel_hi:[1,0,0]
	v_pk_fma_f32 v[152:153], v[40:41], s[56:57], v[60:61] op_sel_hi:[1,0,0]
	v_pk_fma_f32 v[156:157], v[38:39], s[56:57], v[60:61] op_sel_hi:[1,0,0]
	v_pk_fma_f32 v[160:161], v[36:37], s[56:57], v[60:61] op_sel_hi:[1,0,0]
	v_pk_fma_f32 v[162:163], v[34:35], s[56:57], v[60:61] op_sel_hi:[1,0,0]
	v_exp_f32_e32 v166, v18
	v_fmamk_f32 v18, v32, 0x3dd53b94, v60
	v_fmac_f32_e32 v60, 0x3dd53b94, v33
	v_exp_f32_e32 v165, v18
	v_exp_f32_e32 v167, v60
	s_addk_i32 s4, 0x4000
	v_lshl_add_u64 v[18:19], s[18:19], 0, v[50:51]
	v_add_u32_e32 v198, s4, v59
	v_lshl_add_u64 v[184:185], v[18:19], 0, v[54:55]
	v_lshl_add_u64 v[186:187], v[18:19], 0, v[52:53]
	v_mov_b64_e32 v[64:65], v[16:17]
	v_mov_b64_e32 v[48:49], v[16:17]
	v_mov_b64_e32 v[32:33], v[16:17]
	v_mov_b64_e32 v[62:63], v[14:15]
	v_mov_b64_e32 v[60:61], v[12:13]
	v_mov_b64_e32 v[58:59], v[10:11]
	v_mov_b64_e32 v[56:57], v[8:9]
	v_mov_b64_e32 v[54:55], v[6:7]
	v_mov_b64_e32 v[52:53], v[4:5]
	v_mov_b64_e32 v[50:51], v[2:3]
	v_mov_b64_e32 v[46:47], v[14:15]
	v_mov_b64_e32 v[44:45], v[12:13]
	v_mov_b64_e32 v[42:43], v[10:11]
	v_mov_b64_e32 v[40:41], v[8:9]
	v_mov_b64_e32 v[38:39], v[6:7]
	v_mov_b64_e32 v[36:37], v[4:5]
	v_mov_b64_e32 v[34:35], v[2:3]
	v_mov_b64_e32 v[30:31], v[14:15]
	v_mov_b64_e32 v[28:29], v[12:13]
	v_mov_b64_e32 v[26:27], v[10:11]
	v_mov_b64_e32 v[24:25], v[8:9]
	v_mov_b64_e32 v[22:23], v[6:7]
	v_mov_b64_e32 v[20:21], v[4:5]
	v_mov_b64_e32 v[18:19], v[2:3]
	v_and_b32_e32 v230, 63, v0
	v_lshrrev_b32_e32 v231, 6, v0
	v_lshrrev_b32_e32 v232, 4, v0
	v_mul_u32_u24_e32 v232, 0xe00, v232
	v_and_b32_e32 v233, 15, v0
	v_lshl_add_u32 v232, v233, 4, v232
	v_sub_u32_e32 v232, v186, v232
	v_lshrrev_b32_e32 v233, 3, v0
	v_and_b32_e32 v236, 7, v0
	v_lshlrev_b32_e32 v236, 4, v236
	v_lshl_add_u32 v233, v233, 7, v236
	v_sub_u32_e32 v233, v182, v233
	v_add_u32_e32 v232, 0x39d1dc00, v232
	v_add_u32_e32 v233, 0x39b15600, v233
	v_mov_b32_e32 v243, 0
	v_mov_b32_e32 v244, 0x2000
	v_mov_b32_e32 v245, 0x38000
	v_bfe_u32 v236, v230, 2, 3
	v_lshl_add_u32 v236, v231, 3, v236
	v_and_b32_e32 v237, 0xfffffff3, v236
	v_and_b32_e32 v238, 4, v236
	v_lshl_or_b32 v237, v238, 1, v237
	v_and_b32_e32 v238, 8, v236
	v_lshrrev_b32_e32 v238, 1, v238
	v_or_b32_e32 v237, v237, v238
	v_add_u32_e32 v237, 64, v237
	v_mul_u32_u24_e32 v237, 0xe00, v237
	v_add_u32_e32 v237, v237, v232
	v_lshrrev_b32_e32 v238, 5, v230
	v_lshlrev_b32_e32 v238, 6, v238
	v_and_b32_e32 v239, 3, v230
	v_lshl_add_u32 v238, v239, 4, v238
	v_add_u32_e32 v237, v237, v238
	v_add_u32_e32 v242, 0x100, v237
	v_lshl_add_u64 v[206:207], s[14:15], 0, v[242:243]
	v_mov_b32_e32 v236, v230
	v_mul_u32_u24_e32 v237, 0x2ab, v236
	v_lshrrev_b32_e32 v237, 14, v237
	v_mul_u32_u24_e32 v238, 24, v237
	v_sub_u32_e32 v238, v236, v238
	v_lshl_add_u32 v237, v231, 3, v237
	v_bfe_u32 v239, v237, 1, 3
	v_xor_b32_e32 v238, v238, v239
	v_add_u32_e32 v237, 0x80, v237
	v_mul_u32_u24_e32 v240, 0xe00, v237
	v_add_u32_e32 v240, v240, v232
	v_lshl_add_u32 v240, v238, 4, v240
	v_lshl_add_u32 v241, v237, 7, v233
	v_lshl_add_u32 v241, v238, 4, v241
	v_subrev_u32_e32 v241, 0x100, v241
	v_cmp_gt_u32_e32 vcc, 16, v238
	s_nop 1
	v_cndmask_b32_e32 v242, v241, v240, vcc
	v_cndmask_b32_e32 v205, v244, v245, vcc
	v_lshl_add_u64 v[182:183], s[14:15], 0, v[242:243]
	v_add_u32_e32 v236, 0x40, v230
	v_mul_u32_u24_e32 v237, 0x2ab, v236
	v_lshrrev_b32_e32 v237, 14, v237
	v_mul_u32_u24_e32 v238, 24, v237
	v_sub_u32_e32 v238, v236, v238
	v_lshl_add_u32 v237, v231, 3, v237
	v_bfe_u32 v239, v237, 1, 3
	v_xor_b32_e32 v238, v238, v239
	v_add_u32_e32 v237, 0x80, v237
	v_mul_u32_u24_e32 v240, 0xe00, v237
	v_add_u32_e32 v240, v240, v232
	v_lshl_add_u32 v240, v238, 4, v240
	v_lshl_add_u32 v241, v237, 7, v233
	v_lshl_add_u32 v241, v238, 4, v241
	v_subrev_u32_e32 v241, 0x100, v241
	v_cmp_gt_u32_e32 vcc, 16, v238
	s_nop 1
	v_cndmask_b32_e32 v242, v241, v240, vcc
	v_cndmask_b32_e32 v208, v244, v245, vcc
	v_lshl_add_u64 v[184:185], s[14:15], 0, v[242:243]
	v_add_u32_e32 v236, 0x80, v230
	v_mul_u32_u24_e32 v237, 0x2ab, v236
	v_lshrrev_b32_e32 v237, 14, v237
	v_mul_u32_u24_e32 v238, 24, v237
	v_sub_u32_e32 v238, v236, v238
	v_lshl_add_u32 v237, v231, 3, v237
	v_bfe_u32 v239, v237, 1, 3
	v_xor_b32_e32 v238, v238, v239
	v_add_u32_e32 v237, 0x80, v237
	v_mul_u32_u24_e32 v240, 0xe00, v237
	v_add_u32_e32 v240, v240, v232
	v_lshl_add_u32 v240, v238, 4, v240
	v_lshl_add_u32 v241, v237, 7, v233
	v_lshl_add_u32 v241, v238, 4, v241
	v_subrev_u32_e32 v241, 0x100, v241
	v_cmp_gt_u32_e32 vcc, 16, v238
	s_nop 1
	v_cndmask_b32_e32 v242, v241, v240, vcc
	v_cndmask_b32_e32 v209, v244, v245, vcc
	v_lshl_add_u64 v[186:187], s[14:15], 0, v[242:243]
	v_readfirstlane_b32 s98, v0
	s_nop 3
	s_lshr_b32 s98, s98, 8
	s_setprio 0
	s_cmp_lg_u32 s98, 0
	s_cbranch_scc0 .Latt_prio_done
	s_setprio 1

.LBB0_1356:
	s_setprio 0
	s_cmp_eq_u32 s98, 0
	s_cbranch_scc0 .Latt_prio_back
	s_setprio 1
.Latt_prio_back:
	s_nop 0
	v_readfirstlane_b32 s4, v0
	s_nop 0
	s_lshl_b32 s5, s4, 4
	s_lshl_b32 s5, s5, 1
	s_add_i32 m0, s5, 0x4000
	s_nop 0
	global_load_lds_dwordx4 v[206:207], off
	s_add_i32 m0, s5, 0x4380
	s_nop 0
	global_load_lds_dwordx4 v[206:207], off offset:128
	ds_read_b128 v[182:185], v203 offset:24576
	ds_read_b128 v[206:209], v203 offset:36864
	ds_read_b128 v[230:233], v204 offset:24576
	ds_read_b128 v[236:239], v204 offset:36864
	ds_read_b128 v[66:69], v201 offset:36864
	ds_read_b128 v[70:73], v201 offset:24576
	s_waitcnt lgkmcnt(0)
	v_mfma_f32_32x32x16_bf16 v[82:97], v[70:73], v[128:131], 0
	v_mfma_f32_32x32x16_bf16 v[82:97], v[182:185], v[124:127], v[82:97]
	v_mfma_f32_32x32x16_bf16 v[66:81], v[66:69], v[128:131], 0
	ds_read_b128 v[128:131], v202 offset:24576
	ds_read_b128 v[240:243], v202 offset:36864
	v_mfma_f32_32x32x16_bf16 v[82:97], v[230:233], v[120:123], v[82:97]
	v_mfma_f32_32x32x16_bf16 v[66:81], v[206:209], v[124:127], v[66:81]
	ds_read_b128 v[124:127], v201 offset:24704
	ds_read_b128 v[182:185], v201 offset:36992
	s_waitcnt lgkmcnt(3)
	v_mfma_f32_32x32x16_bf16 v[82:97], v[128:131], v[116:119], v[82:97]
	v_mfma_f32_32x32x16_bf16 v[66:81], v[236:239], v[120:123], v[66:81]
	ds_read_b128 v[120:123], v203 offset:24704
	ds_read_b128 v[206:209], v203 offset:36992
	s_waitcnt lgkmcnt(3)
	v_mfma_f32_32x32x16_bf16 v[82:97], v[124:127], v[112:115], v[82:97]
	v_mfma_f32_32x32x16_bf16 v[66:81], v[240:243], v[116:119], v[66:81]
	ds_read_b128 v[116:119], v204 offset:24704
	ds_read_b128 v[128:131], v204 offset:36992
	s_waitcnt lgkmcnt(3)
	v_mfma_f32_32x32x16_bf16 v[82:97], v[120:123], v[108:111], v[82:97]
	v_mfma_f32_32x32x16_bf16 v[66:81], v[182:185], v[112:115], v[66:81]
	ds_read_b128 v[112:115], v202 offset:24704
	ds_read_b128 v[124:127], v202 offset:36992
	s_waitcnt lgkmcnt(3)
	v_mfma_f32_32x32x16_bf16 v[82:97], v[116:119], v[104:107], v[82:97]
	v_mfma_f32_32x32x16_bf16 v[66:81], v[206:209], v[108:111], v[66:81]
	ds_read_b128 v[108:111], v201 offset:24832
	ds_read_b128 v[120:123], v201 offset:37120
	s_waitcnt lgkmcnt(3)
	v_mfma_f32_32x32x16_bf16 v[82:97], v[112:115], v[100:103], v[82:97]
	v_mfma_f32_32x32x16_bf16 v[66:81], v[128:131], v[104:107], v[66:81]
	ds_read_b128 v[104:107], v203 offset:24832
	ds_read_b128 v[116:119], v203 offset:37120
	s_waitcnt lgkmcnt(3)
	v_mfma_f32_32x32x16_bf16 v[82:97], v[108:111], v[144:147], v[82:97]
	v_mfma_f32_32x32x16_bf16 v[66:81], v[124:127], v[100:103], v[66:81]
	ds_read_b128 v[100:103], v204 offset:24832
	ds_read_b128 v[112:115], v204 offset:37120
	v_exp_f32_e32 v124, v148
	v_exp_f32_e32 v125, v149
	s_waitcnt lgkmcnt(3)
	v_mfma_f32_32x32x16_bf16 v[82:97], v[104:107], v[140:143], v[82:97]
	v_mfma_f32_32x32x16_bf16 v[66:81], v[120:123], v[144:147], v[66:81]
	ds_read_b128 v[108:111], v202 offset:24832
	ds_read_b128 v[120:123], v202 offset:37120
	s_waitcnt lgkmcnt(3)
	v_mfma_f32_32x32x16_bf16 v[82:97], v[100:103], v[136:139], v[82:97]
	v_add_f32_e32 v100, 0, v169
	v_add_f32_e32 v100, v191, v100
	v_add_f32_e32 v100, v170, v100
	v_add_f32_e32 v100, v192, v100
	v_add_f32_e32 v100, v190, v100
	v_add_f32_e32 v100, v193, v100
	v_add_f32_e32 v100, v171, v100
	v_mfma_f32_32x32x16_bf16 v[66:81], v[116:119], v[140:143], v[66:81]
	v_add_f32_e32 v100, v189, v100
	v_add_f32_e32 v100, v173, v100
	v_add_f32_e32 v100, v175, v100
	v_add_f32_e32 v100, v174, v100
	v_add_f32_e32 v100, v188, v100
	v_add_f32_e32 v100, v164, v100
	v_add_f32_e32 v100, v166, v100
	s_waitcnt lgkmcnt(1)
	v_mfma_f32_32x32x16_bf16 v[82:97], v[108:111], v[132:135], v[82:97]
	v_exp_f32_e32 v110, v162
	v_exp_f32_e32 v111, v163
	v_add_f32_e32 v100, v165, v100
	v_add_f32_e32 v100, v167, v100
	v_add_f32_e32 v100, v110, v100
	v_add_f32_e32 v100, v111, v100
	v_exp_f32_e32 v116, v152
	v_mfma_f32_32x32x16_bf16 v[66:81], v[112:115], v[136:139], v[66:81]
	v_exp_f32_e32 v112, v160
	v_exp_f32_e32 v113, v161
	v_exp_f32_e32 v114, v156
	v_exp_f32_e32 v115, v157
	v_add_f32_e32 v100, v112, v100
	v_exp_f32_e32 v117, v153
	v_add_f32_e32 v100, v113, v100
	v_exp_f32_e32 v118, v150
	v_add_f32_e32 v100, v114, v100
	v_exp_f32_e32 v119, v151
	v_add_f32_e32 v100, v115, v100
	s_waitcnt lgkmcnt(0)
	v_mfma_f32_32x32x16_bf16 v[66:81], v[120:123], v[132:135], v[66:81]
	v_exp_f32_e32 v120, v158
	v_add_f32_e32 v100, v116, v100
	v_exp_f32_e32 v121, v159
	v_add_f32_e32 v100, v117, v100
	v_exp_f32_e32 v122, v154
	v_add_f32_e32 v100, v118, v100
	v_exp_f32_e32 v123, v155
	v_add_f32_e32 v100, v119, v100
	v_add_f32_e32 v100, v120, v100
	v_add_f32_e32 v100, v121, v100
	v_add_f32_e32 v100, v122, v100
	v_add_f32_e32 v100, v123, v100
	v_add_f32_e32 v100, v124, v100
	v_add_f32_e32 v104, v125, v100
	v_mov_b32_e32 v105, v104
	v_cvt_pk_bf16_f32 v100, v169, v191
	v_cvt_pk_bf16_f32 v101, v170, v192
	v_cvt_pk_bf16_f32 v102, v190, v193
	v_cvt_pk_bf16_f32 v103, v171, v189
	s_nop 1
	v_permlane32_swap_b32_e32 v104, v105
	v_permlane32_swap_b32_e32 v100, v102
	v_permlane32_swap_b32_e32 v101, v103
	v_cvt_pk_bf16_f32 v106, v173, v175
	v_cvt_pk_bf16_f32 v107, v174, v188
	v_cvt_pk_bf16_f32 v108, v164, v166
	v_cvt_pk_bf16_f32 v109, v165, v167
	v_cvt_pk_bf16_f32 v110, v110, v111
	v_cvt_pk_bf16_f32 v111, v112, v113
	v_cvt_pk_bf16_f32 v112, v114, v115
	v_cvt_pk_bf16_f32 v113, v116, v117
	v_cvt_pk_bf16_f32 v114, v118, v119
	v_cvt_pk_bf16_f32 v115, v120, v121
	v_cvt_pk_bf16_f32 v116, v122, v123
	v_cvt_pk_bf16_f32 v117, v124, v125
	s_nop 0
	v_permlane32_swap_b32_e32 v106, v108
	v_permlane32_swap_b32_e32 v107, v109
	v_permlane32_swap_b32_e32 v110, v112
	v_permlane32_swap_b32_e32 v111, v113
	v_permlane32_swap_b32_e32 v114, v116
	v_permlane32_swap_b32_e32 v115, v117
	ds_read_b64_tr_b16 v[118:119], v200 offset:0
	ds_read_b64_tr_b16 v[120:121], v200 offset:0x800
	ds_read_b64_tr_b16 v[122:123], v200 offset:0x1000
	ds_read_b64_tr_b16 v[124:125], v200 offset:0x1800
	ds_read_b64_tr_b16 v[126:127], v200 offset:0x2000
	ds_read_b64_tr_b16 v[128:129], v200 offset:0x2800
	ds_read_b64_tr_b16 v[130:131], v200 offset:0x3000
	ds_read_b64_tr_b16 v[132:133], v200 offset:0x3800
	s_waitcnt lgkmcnt(0)
	s_nop 0
	v_mfma_f32_32x32x16_bf16 v[2:17], v[100:103], v[118:121], v[2:17]
	ds_read_b64_tr_b16 v[118:119], v200 offset:0x200
	ds_read_b64_tr_b16 v[120:121], v200 offset:0xa00
	v_mfma_f32_32x32x16_bf16 v[2:17], v[106:109], v[122:125], v[2:17]
	ds_read_b64_tr_b16 v[122:123], v200 offset:0x1200
	ds_read_b64_tr_b16 v[124:125], v200 offset:0x1a00
	v_mfma_f32_32x32x16_bf16 v[2:17], v[110:113], v[126:129], v[2:17]
	ds_read_b64_tr_b16 v[126:127], v200 offset:0x2200
	ds_read_b64_tr_b16 v[128:129], v200 offset:0x2a00
	v_mfma_f32_32x32x16_bf16 v[2:17], v[114:117], v[130:133], v[2:17]
	ds_read_b64_tr_b16 v[130:131], v200 offset:0x3200
	ds_read_b64_tr_b16 v[132:133], v200 offset:0x3a00
	s_waitcnt lgkmcnt(0)
	v_mfma_f32_32x32x16_bf16 v[50:65], v[100:103], v[118:121], v[50:65]
	ds_read_b64_tr_b16 v[118:119], v200 offset:0x400
	ds_read_b64_tr_b16 v[120:121], v200 offset:0xc00
	v_mfma_f32_32x32x16_bf16 v[50:65], v[106:109], v[122:125], v[50:65]
	ds_read_b64_tr_b16 v[122:123], v200 offset:0x1400
	ds_read_b64_tr_b16 v[124:125], v200 offset:0x1c00
	v_mfma_f32_32x32x16_bf16 v[50:65], v[110:113], v[126:129], v[50:65]
	ds_read_b64_tr_b16 v[126:127], v200 offset:0x2400
	ds_read_b64_tr_b16 v[128:129], v200 offset:0x2c00
	v_mfma_f32_32x32x16_bf16 v[50:65], v[114:117], v[130:133], v[50:65]
	ds_read_b64_tr_b16 v[130:131], v200 offset:0x3400
	ds_read_b64_tr_b16 v[132:133], v200 offset:0x3c00
	s_waitcnt lgkmcnt(0)
	v_mfma_f32_32x32x16_bf16 v[34:49], v[100:103], v[118:121], v[34:49]
	ds_read_b64_tr_b16 v[118:119], v200 offset:0x600
	ds_read_b64_tr_b16 v[120:121], v200 offset:0xe00
	v_mfma_f32_32x32x16_bf16 v[34:49], v[106:109], v[122:125], v[34:49]
	ds_read_b64_tr_b16 v[122:123], v200 offset:0x1600
	ds_read_b64_tr_b16 v[124:125], v200 offset:0x1e00
	v_mfma_f32_32x32x16_bf16 v[34:49], v[110:113], v[126:129], v[34:49]
	ds_read_b64_tr_b16 v[126:127], v200 offset:0x2600
	ds_read_b64_tr_b16 v[128:129], v200 offset:0x2e00
	v_mfma_f32_32x32x16_bf16 v[34:49], v[114:117], v[130:133], v[34:49]
	ds_read_b64_tr_b16 v[130:131], v200 offset:0x3600
	ds_read_b64_tr_b16 v[132:133], v200 offset:0x3e00
	s_waitcnt lgkmcnt(0)
	v_mfma_f32_32x32x16_bf16 v[18:33], v[100:103], v[118:121], v[18:33]
	v_max_f32_e32 v100, v83, v83
	v_max_f32_e32 v101, v82, v82
	v_max_f32_e32 v100, v101, v100
	v_max3_f32 v100, v100, v84, v85
	v_max3_f32 v100, v100, v86, v87
	v_max3_f32 v100, v100, v88, v89
	v_max3_f32 v100, v100, v90, v91
	v_max3_f32 v100, v100, v92, v93
	v_max3_f32 v100, v100, v94, v95
	v_mfma_f32_32x32x16_bf16 v[18:33], v[106:109], v[122:125], v[18:33]
	v_max3_f32 v100, v100, v96, v97
	v_max3_f32 v100, v100, v66, v67
	v_max3_f32 v100, v100, v68, v69
	v_max3_f32 v100, v100, v70, v71
	v_max3_f32 v100, v100, v72, v73
	v_max3_f32 v100, v100, v74, v75
	v_max3_f32 v100, v100, v76, v77
	v_max3_f32 v100, v100, v78, v79
	v_mfma_f32_32x32x16_bf16 v[18:33], v[110:113], v[126:129], v[18:33]
	v_max3_f32 v100, v100, v80, v81
	v_mov_b32_e32 v101, v100
	s_nop 1
	v_permlane32_swap_b32_e32 v100, v101
	v_max_f32_e32 v101, v101, v101
	v_max_f32_e32 v100, v100, v100
	v_max_f32_e32 v100, v100, v101
	v_sub_f32_e32 v101, v100, v211
	v_cmp_ge_f32_e32 vcc, s11, v101
	v_max_f32_e32 v101, v211, v211
	v_max_f32_e32 v100, v101, v100
	v_mfma_f32_32x32x16_bf16 v[18:33], v[114:117], v[130:133], v[18:33]
	v_sub_f32_e32 v101, v211, v100
	v_mul_f32_e32 v101, 0x3dd53b94, v101
	v_exp_f32_e32 v101, v101
	s_cmp_eq_u64 vcc, exec
	s_cselect_b64 s[18:19], -1, 0
	v_mov_b32_e32 v229, v228
	v_cndmask_b32_e64 v102, v101, 1.0, s[18:19]
	v_cmp_gt_f32_e32 vcc, 1.0, v102
	s_waitcnt vmcnt(0)
	s_barrier
	s_cbranch_vccz .LBB0_1360
	s_and_saveexec_b64 s[4:5], s[0:1]
	ds_write_b32 v197, v102 offset:128
	s_or_b64 exec, exec, s[4:5]
	s_waitcnt lgkmcnt(0)
	v_add_u32_e32 v101, v196, v98
	ds_read_b128 v[106:109], v101 offset:224
	ds_read_b128 v[110:113], v101 offset:192
	ds_read_b128 v[114:117], v101 offset:160
	ds_read_b128 v[118:121], v101 offset:128
	s_waitcnt lgkmcnt(3)
	v_pk_mul_f32 v[14:15], v[14:15], v[106:107]
	s_waitcnt lgkmcnt(2)
	v_pk_mul_f32 v[10:11], v[10:11], v[110:111]
	s_waitcnt lgkmcnt(1)
	v_pk_mul_f32 v[6:7], v[6:7], v[114:115]
	v_pk_mul_f32 v[16:17], v[16:17], v[108:109]
	v_pk_mul_f32 v[12:13], v[12:13], v[112:113]
	v_pk_mul_f32 v[8:9], v[8:9], v[116:117]
	s_waitcnt lgkmcnt(0)
	v_pk_mul_f32 v[4:5], v[4:5], v[120:121]
	v_pk_mul_f32 v[2:3], v[2:3], v[118:119]
	v_pk_mul_f32 v[62:63], v[62:63], v[106:107]
	v_pk_mul_f32 v[58:59], v[58:59], v[110:111]
	v_pk_mul_f32 v[54:55], v[54:55], v[114:115]
	v_pk_mul_f32 v[64:65], v[64:65], v[108:109]
	v_pk_mul_f32 v[60:61], v[60:61], v[112:113]
	v_pk_mul_f32 v[56:57], v[56:57], v[116:117]
	v_pk_mul_f32 v[52:53], v[52:53], v[120:121]
	v_pk_mul_f32 v[50:51], v[50:51], v[118:119]
	v_pk_mul_f32 v[46:47], v[46:47], v[106:107]
	v_pk_mul_f32 v[42:43], v[42:43], v[110:111]
	v_pk_mul_f32 v[38:39], v[38:39], v[114:115]
	v_pk_mul_f32 v[48:49], v[48:49], v[108:109]
	v_pk_mul_f32 v[44:45], v[44:45], v[112:113]
	v_pk_mul_f32 v[40:41], v[40:41], v[116:117]
	v_pk_mul_f32 v[36:37], v[36:37], v[120:121]
	v_pk_mul_f32 v[34:35], v[34:35], v[118:119]
	v_pk_mul_f32 v[30:31], v[30:31], v[106:107]
	v_pk_mul_f32 v[26:27], v[26:27], v[110:111]
	v_pk_mul_f32 v[22:23], v[22:23], v[114:115]
	v_pk_mul_f32 v[32:33], v[32:33], v[108:109]
	v_pk_mul_f32 v[28:29], v[28:29], v[112:113]
	v_pk_mul_f32 v[24:25], v[24:25], v[116:117]
	v_pk_mul_f32 v[20:21], v[20:21], v[120:121]
	v_pk_mul_f32 v[18:19], v[18:19], v[118:119]
